# MoE GEMM tile loops: panel->expert table staged in LDS once per phase instead of a global load with a full vmcnt drain per tile
# baseline (speedup 1.0000x reference)
.LBB0_1478:
	s_waitcnt lgkmcnt(0)
	global_load_dword v0, v239, s[8:9] offset:640
	s_mov_b64 s[4:5], 0x100
	s_add_u32 s10, s8, 0x781000
	s_mov_b64 s[18:19], 0x17000000
	s_mov_b32 s48, -1
	s_mov_b64 s[20:21], 0x740000
	s_addc_u32 s11, s9, 0
	v_mbcnt_lo_u32_b32 v5, -1, 0
	v_mbcnt_hi_u32_b32 v5, -1, v5
	v_lshlrev_b32_e32 v5, 2, v5
	global_load_dword v6, v5, s[10:11]
	global_load_dword v7, v5, s[10:11] offset:256
	global_load_dword v8, v5, s[10:11] offset:512
	s_mov_b32 s2, s6
	s_waitcnt vmcnt(0)
	v_readfirstlane_b32 s5, v0
	v_add_u32_e32 v5, 0x21000, v5
	ds_write_b32 v5, v6
	ds_write_b32 v5, v7 offset:256
	ds_write_b32 v5, v8 offset:512
	s_waitcnt lgkmcnt(0)
	s_mul_i32 s12, s5, 22

.LBB0_1498:
	s_ashr_i32 s22, s28, 3
	s_add_i32 s22, s30, s22
	s_mul_hi_i32 s23, s22, 0x2e8ba2e9
	s_lshr_b32 s28, s23, 31
	s_ashr_i32 s23, s23, 5
	s_add_i32 s23, s23, s28
	s_lshl_b32 s28, s23, 3
	s_sub_i32 s29, s5, s28
	s_min_i32 s29, s29, 8
	s_abs_i32 s30, s29
	v_cvt_f32_u32_e32 v0, s30
	s_sub_i32 s34, 0, s30
	s_mulk_i32 s23, 0xb0
	s_sub_i32 s23, s22, s23
	v_rcp_iflag_f32_e32 v0, v0
	s_abs_i32 s22, s23
	s_xor_b32 s31, s23, s29
	s_ashr_i32 s31, s31, 31
	v_mul_f32_e32 v0, 0x4f7ffffe, v0
	v_cvt_u32_f32_e32 v0, v0
	s_mov_b32 s64, 0
	v_readfirstlane_b32 s35, v0
	s_mul_i32 s34, s34, s35
	s_mul_hi_u32 s34, s35, s34
	s_add_i32 s35, s35, s34
	s_mul_hi_u32 s34, s22, s35
	s_mul_i32 s35, s34, s30
	s_sub_i32 s22, s22, s35
	s_add_i32 s44, s34, 1
	s_sub_i32 s35, s22, s30
	s_cmp_ge_u32 s22, s30
	s_cselect_b32 s34, s44, s34
	s_cselect_b32 s22, s35, s22
	s_add_i32 s35, s34, 1
	s_cmp_ge_u32 s22, s30
	s_cselect_b32 s22, s35, s34
	s_xor_b32 s22, s22, s31
	s_sub_i32 s22, s22, s31
	s_mul_i32 s29, s22, s29
	s_sub_i32 s23, s23, s29
	s_andn2_b64 vcc, exec, s[16:17]
	s_add_i32 s28, s28, s23
	s_cbranch_vccnz .LBB0_1500
	s_lshl_b32 s30, s28, 2
	s_add_i32 s30, s30, 0x21000
	v_mov_b32_e32 v0, s30
	ds_read_b32 v0, v0
	s_waitcnt lgkmcnt(0)
	v_readfirstlane_b32 s64, v0

.LBB0_1574:
	s_load_dwordx2 s[14:15], s[4:5], 0xc8
	s_andn2_b64 vcc, exec, s[8:9]
	s_cbranch_vccnz .LBB0_1576
	s_waitcnt lgkmcnt(0)
	global_load_dword v0, v239, s[14:15] offset:640
	s_mov_b64 s[12:13], 0x100
	s_add_u32 s4, s14, 0x781000
	s_mov_b32 s40, -1
	s_addc_u32 s5, s15, 0
	v_mbcnt_lo_u32_b32 v5, -1, 0
	v_mbcnt_hi_u32_b32 v5, -1, v5
	v_lshlrev_b32_e32 v5, 2, v5
	global_load_dword v6, v5, s[4:5]
	global_load_dword v7, v5, s[4:5] offset:256
	global_load_dword v8, v5, s[4:5] offset:512
	s_mov_b32 s2, s3
	s_waitcnt vmcnt(0)
	v_readfirstlane_b32 s13, v0
	v_add_u32_e32 v5, 0x21000, v5
	ds_write_b32 v5, v6
	ds_write_b32 v5, v7 offset:256
	ds_write_b32 v5, v8 offset:512
	s_waitcnt lgkmcnt(0)
	s_lshl_b32 s10, s13, 2
	s_branch .LBB0_1577

.LBB0_1600:
	s_ashr_i32 s22, s26, 3
	s_add_i32 s22, s28, s22
	s_ashr_i32 s23, s22, 31
	s_lshr_b32 s23, s23, 27
	s_add_i32 s26, s22, s23
	s_ashr_i32 s23, s26, 5
	s_lshl_b32 s27, s23, 3
	s_sub_i32 s23, s13, s27
	s_min_i32 s28, s23, 8
	s_abs_i32 s29, s28
	v_cvt_f32_u32_e32 v0, s29
	s_sub_i32 s59, 0, s29
	s_andn2_b32 s26, s26, 31
	s_sub_i32 s22, s22, s26
	v_rcp_iflag_f32_e32 v0, v0
	s_abs_i32 s26, s22
	s_xor_b32 s57, s22, s28
	s_ashr_i32 s57, s57, 31
	v_mul_f32_e32 v0, 0x4f7ffffe, v0
	v_cvt_u32_f32_e32 v0, v0
	s_mov_b32 s23, 0
	v_readfirstlane_b32 s60, v0
	s_mul_i32 s59, s59, s60
	s_mul_hi_u32 s59, s60, s59
	s_add_i32 s60, s60, s59
	s_mul_hi_u32 s59, s26, s60
	s_mul_i32 s60, s59, s29
	s_sub_i32 s26, s26, s60
	s_add_i32 s61, s59, 1
	s_sub_i32 s60, s26, s29
	s_cmp_ge_u32 s26, s29
	s_cselect_b32 s59, s61, s59
	s_cselect_b32 s26, s60, s26
	s_add_i32 s60, s59, 1
	s_cmp_ge_u32 s26, s29
	s_cselect_b32 s26, s60, s59
	s_xor_b32 s26, s26, s57
	s_sub_i32 s57, s26, s57
	s_mul_i32 s26, s57, s28
	s_sub_i32 s22, s22, s26
	s_andn2_b64 vcc, exec, s[20:21]
	s_add_i32 s22, s27, s22
	s_cbranch_vccnz .LBB0_1602
	s_lshl_b32 s26, s22, 2
	s_add_i32 s26, s26, 0x21000
	v_mov_b32_e32 v0, s26
	ds_read_b32 v0, v0
	s_waitcnt lgkmcnt(0)
	v_readfirstlane_b32 s23, v0
